# k_bscatter: the wave that is idle during the offsets phase touches the block's src/dst/w lines at kernel entry so the real edge loads three barriers later hit L2
# baseline (speedup 1.0000x reference)
_Z10k_bscatterPKiS0_PKfS0_PiP15HIP_vector_typeIiLj2EE:
	v_readfirstlane_b32 s43, v0
	s_nop 3
	s_cmpk_ge_u32 s43, 0x3c0
	s_cbranch_scc0 .Lbs_nopf
	s_load_dwordx2 s[36:37], s[0:1], 0x0
	s_load_dwordx2 s[38:39], s[0:1], 0x8
	s_load_dwordx2 s[40:41], s[0:1], 0x10
	s_mul_i32 s42, s2, 0x3d0c
	v_and_b32_e32 v89, 63, v0
	v_lshlrev_b32_e32 v89, 6, v89
	v_add_u32_e32 v89, s42, v89
	s_waitcnt lgkmcnt(0)
	v_add_u32_e32 v90, 0x0, v89
	v_min_u32_e32 v90, 0x3d08fc, v90
	global_load_dword v92, v90, s[36:37]
	global_load_dword v93, v90, s[38:39]
	global_load_dword v94, v90, s[40:41]
	v_add_u32_e32 v90, 0x1000, v89
	v_min_u32_e32 v90, 0x3d08fc, v90
	global_load_dword v95, v90, s[36:37]
	global_load_dword v96, v90, s[38:39]
	global_load_dword v97, v90, s[40:41]
	v_add_u32_e32 v90, 0x2000, v89
	v_min_u32_e32 v90, 0x3d08fc, v90
	global_load_dword v98, v90, s[36:37]
	global_load_dword v99, v90, s[38:39]
	global_load_dword v100, v90, s[40:41]
	v_add_u32_e32 v90, 0x3000, v89
	v_min_u32_e32 v90, 0x3d08fc, v90
	global_load_dword v101, v90, s[36:37]
	global_load_dword v102, v90, s[38:39]
	global_load_dword v103, v90, s[40:41]
.Lbs_nopf:
	s_load_dwordx2 s[16:17], s[0:1], 0x8
	s_load_dwordx4 s[24:27], s[0:1], 0x20
	s_movk_i32 s3, 0x3ae
	v_cmp_gt_u32_e32 vcc, s3, v0
	s_and_saveexec_b64 s[4:5], vcc
	s_cbranch_execz .LBB0_88
	v_mul_u32_u24_e32 v1, 0x343, v0
	s_load_dwordx2 s[6:7], s[0:1], 0x18
	v_lshrrev_b32_e32 v1, 17, v1
	v_mul_lo_u16_e32 v3, 43, v1
	v_min_u32_e32 v4, 0xd5, v3
	v_mul_lo_u16_e32 v2, 0x9d, v1
	v_add_u32_e32 v6, 43, v4
	v_sub_u16_e32 v2, v0, v2
	v_cmp_gt_u32_e32 vcc, v6, v3
	v_mov_b32_e32 v4, 0
	v_mov_b32_e32 v5, 0
	s_and_saveexec_b64 s[8:9], vcc
	s_cbranch_execz .LBB0_3
	v_mul_u32_u24_e32 v5, 0x9d, v3
	v_add_lshl_u32 v5, v5, v2, 2
	s_waitcnt lgkmcnt(0)
	global_load_dword v5, v5, s[6:7]

	.amdhsa_kernel _Z10k_bscatterPKiS0_PKfS0_PiP15HIP_vector_typeIiLj2EE
		.amdhsa_group_segment_fixed_size 56512
		.amdhsa_private_segment_fixed_size 0
		.amdhsa_kernarg_size 48
		.amdhsa_user_sgpr_count 2
		.amdhsa_user_sgpr_dispatch_ptr 0
		.amdhsa_user_sgpr_queue_ptr 0
		.amdhsa_user_sgpr_kernarg_segment_ptr 1
		.amdhsa_user_sgpr_dispatch_id 0
		.amdhsa_user_sgpr_kernarg_preload_length 0
		.amdhsa_user_sgpr_kernarg_preload_offset 0
		.amdhsa_user_sgpr_private_segment_size 0
		.amdhsa_uses_dynamic_stack 0
		.amdhsa_enable_private_segment 0
		.amdhsa_system_sgpr_workgroup_id_x 1
		.amdhsa_system_sgpr_workgroup_id_y 0
		.amdhsa_system_sgpr_workgroup_id_z 0
		.amdhsa_system_sgpr_workgroup_info 0
		.amdhsa_system_vgpr_workitem_id 0
		.amdhsa_next_free_vgpr 104
		.amdhsa_next_free_sgpr 44
		.amdhsa_accum_offset 104
		.amdhsa_reserve_vcc 1
		.amdhsa_float_round_mode_32 0
		.amdhsa_float_round_mode_16_64 0
		.amdhsa_float_denorm_mode_32 3
		.amdhsa_float_denorm_mode_16_64 3
		.amdhsa_dx10_clamp 1
		.amdhsa_ieee_mode 1
		.amdhsa_fp16_overflow 0
		.amdhsa_tg_split 0
		.amdhsa_exception_fp_ieee_invalid_op 0
		.amdhsa_exception_fp_denorm_src 0
		.amdhsa_exception_fp_ieee_div_zero 0
		.amdhsa_exception_fp_ieee_overflow 0
		.amdhsa_exception_fp_ieee_underflow 0
		.amdhsa_exception_fp_ieee_inexact 0
		.amdhsa_exception_int_div_zero 0
	.end_amdhsa_kernel

amdhsa.kernels:
  - .agpr_count:     0
    .args:
      - .actual_access:  read_only
        .address_space:  global
        .offset:         0
        .size:           8
        .value_kind:     global_buffer
      - .actual_access:  read_only
        .address_space:  global
        .offset:         8
        .size:           8
        .value_kind:     global_buffer
      - .actual_access:  read_only
        .address_space:  global
        .offset:         16
        .size:           8
        .value_kind:     global_buffer
      - .actual_access:  read_only
        .address_space:  global
        .offset:         24
        .size:           8
        .value_kind:     global_buffer
      - .actual_access:  write_only
        .address_space:  global
        .offset:         32
        .size:           8
        .value_kind:     global_buffer
      - .actual_access:  write_only
        .address_space:  global
        .offset:         40
        .size:           8
        .value_kind:     global_buffer
    .group_segment_fixed_size: 56512
    .kernarg_segment_align: 8
    .kernarg_segment_size: 48
    .language:       OpenCL C
    .language_version:
      - 2
      - 0
    .max_flat_workgroup_size: 1024
    .name:           _Z10k_bscatterPKiS0_PKfS0_PiP15HIP_vector_typeIiLj2EE
    .private_segment_fixed_size: 0
    .sgpr_count:     50
    .sgpr_spill_count: 0
    .symbol:         _Z10k_bscatterPKiS0_PKfS0_PiP15HIP_vector_typeIiLj2EE.kd
    .uniform_work_group_size: 1
    .uses_dynamic_stack: false
    .vgpr_count:     104
    .vgpr_spill_count: 0
    .wavefront_size: 64
  - .agpr_count:     0
    .args:
      - .actual_access:  read_only
        .address_space:  global
        .offset:         0
        .size:           8
        .value_kind:     global_buffer
      - .actual_access:  read_only
        .address_space:  global
        .offset:         8
        .size:           8
        .value_kind:     global_buffer
      - .actual_access:  write_only
        .address_space:  global
        .offset:         16
        .size:           8
        .value_kind:     global_buffer
      - .actual_access:  write_only
        .address_space:  global
        .offset:         24
        .size:           8
        .value_kind:     global_buffer
      - .actual_access:  write_only
        .address_space:  global
        .offset:         32
        .size:           8
        .value_kind:     global_buffer
      - .actual_access:  write_only
        .address_space:  global
        .offset:         40
        .size:           8
        .value_kind:     global_buffer
      - .actual_access:  read_only
        .address_space:  global
        .offset:         48
        .size:           8
        .value_kind:     global_buffer
      - .actual_access:  write_only
        .address_space:  global
        .offset:         56
        .size:           8
        .value_kind:     global_buffer
    .group_segment_fixed_size: 12352
    .kernarg_segment_align: 8
    .kernarg_segment_size: 64
    .language:       OpenCL C
    .language_version:
      - 2
      - 0
    .max_flat_workgroup_size: 1024
    .name:           _Z8k_bfinalPK15HIP_vector_typeIiLj2EEPKiPS0_PiS6_PfPKfPDF16_
    .private_segment_fixed_size: 0
    .sgpr_count:     38
    .sgpr_spill_count: 0
    .symbol:         _Z8k_bfinalPK15HIP_vector_typeIiLj2EEPKiPS0_PiS6_PfPKfPDF16_.kd
    .uniform_work_group_size: 1
    .uses_dynamic_stack: false
    .vgpr_count:     72
    .vgpr_spill_count: 0
    .wavefront_size: 64
  - .agpr_count:     0
    .args:
      - .actual_access:  read_only
        .address_space:  global
        .offset:         0
        .size:           8
        .value_kind:     global_buffer
      - .actual_access:  write_only
        .address_space:  global
        .offset:         8
        .size:           8
        .value_kind:     global_buffer
      - .actual_access:  write_only
        .address_space:  global
        .offset:         16
        .size:           8
        .value_kind:     global_buffer
      - .actual_access:  read_only
        .address_space:  global
        .offset:         24
        .size:           8
        .value_kind:     global_buffer
      - .actual_access:  read_only
        .address_space:  global
        .offset:         32
        .size:           8
        .value_kind:     global_buffer
      - .actual_access:  write_only
        .address_space:  global
        .offset:         40
        .size:           8
        .value_kind:     global_buffer
      - .actual_access:  read_only
        .address_space:  global
        .offset:         48
        .size:           8
        .value_kind:     global_buffer
      - .actual_access:  read_only
        .address_space:  global
        .offset:         56
        .size:           8
        .value_kind:     global_buffer
      - .actual_access:  read_only
        .address_space:  global
        .offset:         64
        .size:           8
        .value_kind:     global_buffer
      - .actual_access:  read_only
        .address_space:  global
        .offset:         72
        .size:           8
        .value_kind:     global_buffer
      - .actual_access:  read_only
        .address_space:  global
        .offset:         80
        .size:           8
        .value_kind:     global_buffer
      - .actual_access:  read_only
        .address_space:  global
        .offset:         88
        .size:           8
        .value_kind:     global_buffer
      - .actual_access:  write_only
        .address_space:  global
        .offset:         96
        .size:           8
        .value_kind:     global_buffer
      - .actual_access:  write_only
        .address_space:  global
        .offset:         104
        .size:           8
        .value_kind:     global_buffer
      - .actual_access:  write_only
        .address_space:  global
        .offset:         112
        .size:           8
        .value_kind:     global_buffer
      - .actual_access:  write_only
        .address_space:  global
        .offset:         120
        .size:           8
        .value_kind:     global_buffer
      - .actual_access:  write_only
        .address_space:  global
        .offset:         128
        .size:           8
        .value_kind:     global_buffer
    .group_segment_fixed_size: 628
    .kernarg_segment_align: 8
    .kernarg_segment_size: 136
    .language:       OpenCL C
    .language_version:
      - 2
      - 0
    .max_flat_workgroup_size: 1024
    .name:           _Z7k_bhistPKiPiPfPKfS4_PDF16_S4_S4_S4_S4_S4_S4_S5_S5_S5_S5_S2_
    .private_segment_fixed_size: 0
    .sgpr_count:     25
    .sgpr_spill_count: 0
    .symbol:         _Z7k_bhistPKiPiPfPKfS4_PDF16_S4_S4_S4_S4_S4_S4_S5_S5_S5_S5_S2_.kd
    .uniform_work_group_size: 1
    .uses_dynamic_stack: false
    .vgpr_count:     32
    .vgpr_spill_count: 0
    .wavefront_size: 64
  - .agpr_count:     0
    .args:
      - .actual_access:  read_only
        .address_space:  global
        .offset:         0
        .size:           8
        .value_kind:     global_buffer
      - .actual_access:  read_only
        .address_space:  global
        .offset:         8
        .size:           8
        .value_kind:     global_buffer
      - .actual_access:  read_only
        .address_space:  global
        .offset:         16
        .size:           8
        .value_kind:     global_buffer
      - .actual_access:  read_only
        .address_space:  global
        .offset:         24
        .size:           8
        .value_kind:     global_buffer
      - .actual_access:  read_only
        .address_space:  global
        .offset:         32
        .size:           8
        .value_kind:     global_buffer
      - .actual_access:  read_only
        .address_space:  global
        .offset:         40
        .size:           8
        .value_kind:     global_buffer
      - .actual_access:  read_only
        .address_space:  global
        .offset:         48
        .size:           8
        .value_kind:     global_buffer
      - .actual_access:  read_only
        .address_space:  global
        .offset:         56
        .size:           8
        .value_kind:     global_buffer
      - .actual_access:  read_only
        .address_space:  global
        .offset:         64
        .size:           8
        .value_kind:     global_buffer
      - .actual_access:  write_only
        .address_space:  global
        .offset:         72
        .size:           8
        .value_kind:     global_buffer
      - .actual_access:  write_only
        .address_space:  global
        .offset:         80
        .size:           8
        .value_kind:     global_buffer
      - .offset:         88
        .size:           4
        .value_kind:     hidden_block_count_x
      - .offset:         92
        .size:           4
        .value_kind:     hidden_block_count_y
      - .offset:         96
        .size:           4
        .value_kind:     hidden_block_count_z
      - .offset:         100
        .size:           2
        .value_kind:     hidden_group_size_x
      - .offset:         102
        .size:           2
        .value_kind:     hidden_group_size_y
      - .offset:         104
        .size:           2
        .value_kind:     hidden_group_size_z
      - .offset:         106
        .size:           2
        .value_kind:     hidden_remainder_x
      - .offset:         108
        .size:           2
        .value_kind:     hidden_remainder_y
      - .offset:         110
        .size:           2
        .value_kind:     hidden_remainder_z
      - .offset:         128
        .size:           8
        .value_kind:     hidden_global_offset_x
      - .offset:         136
        .size:           8
        .value_kind:     hidden_global_offset_y
      - .offset:         144
        .size:           8
        .value_kind:     hidden_global_offset_z
      - .offset:         152
        .size:           2
        .value_kind:     hidden_grid_dims
    .group_segment_fixed_size: 2048
    .kernarg_segment_align: 8
    .kernarg_segment_size: 344
    .language:       OpenCL C
    .language_version:
      - 2
      - 0
    .max_flat_workgroup_size: 256
    .name:           _Z7k_fold2PKfS0_S0_S0_S0_S0_S0_S0_S0_PDF16_Pf
    .private_segment_fixed_size: 0
    .sgpr_count:     36
    .sgpr_spill_count: 0
    .symbol:         _Z7k_fold2PKfS0_S0_S0_S0_S0_S0_S0_S0_PDF16_Pf.kd
    .uniform_work_group_size: 1
    .uses_dynamic_stack: false
    .vgpr_count:     61
    .vgpr_spill_count: 0
    .wavefront_size: 64
  - .agpr_count:     0
    .args:
      - .actual_access:  read_only
        .address_space:  global
        .offset:         0
        .size:           8
        .value_kind:     global_buffer
      - .actual_access:  read_only
        .address_space:  global
        .offset:         8
        .size:           8
        .value_kind:     global_buffer
      - .actual_access:  write_only
        .address_space:  global
        .offset:         16
        .size:           8
        .value_kind:     global_buffer
      - .actual_access:  read_only
        .address_space:  global
        .offset:         24
        .size:           8
        .value_kind:     global_buffer
      - .actual_access:  read_only
        .address_space:  global
        .offset:         32
        .size:           8
        .value_kind:     global_buffer
      - .actual_access:  read_only
        .address_space:  global
        .offset:         40
        .size:           8
        .value_kind:     global_buffer
      - .actual_access:  read_only
        .address_space:  global
        .offset:         48
        .size:           8
        .value_kind:     global_buffer
      - .actual_access:  read_only
        .address_space:  global
        .offset:         56
        .size:           8
        .value_kind:     global_buffer
      - .actual_access:  read_only
        .address_space:  global
        .offset:         64
        .size:           8
        .value_kind:     global_buffer
      - .actual_access:  read_only
        .address_space:  global
        .offset:         72
        .size:           8
        .value_kind:     global_buffer
      - .actual_access:  read_only
        .address_space:  global
        .offset:         80
        .size:           8
        .value_kind:     global_buffer
      - .actual_access:  write_only
        .address_space:  global
        .offset:         88
        .size:           8
        .value_kind:     global_buffer
      - .actual_access:  write_only
        .address_space:  global
        .offset:         96
        .size:           8
        .value_kind:     global_buffer
      - .address_space:  global
        .offset:         104
        .size:           8
        .value_kind:     global_buffer
      - .actual_access:  write_only
        .address_space:  global
        .offset:         112
        .size:           8
        .value_kind:     global_buffer
      - .actual_access:  read_only
        .address_space:  global
        .offset:         120
        .size:           8
        .value_kind:     global_buffer
      - .actual_access:  read_only
        .address_space:  global
        .offset:         128
        .size:           8
        .value_kind:     global_buffer
    .group_segment_fixed_size: 22272
    .kernarg_segment_align: 8
    .kernarg_segment_size: 136
    .language:       OpenCL C
    .language_version:
      - 2
      - 0
    .max_flat_workgroup_size: 256
    .name:           _Z5k_gcnILi1EEvPKvPK15HIP_vector_typeIiLj2EEPfPKiS8_PKfPKDF16_SA_SA_SA_SA_S6_PDF16_S6_SD_SC_SA_
    .private_segment_fixed_size: 0
    .sgpr_count:     35
    .sgpr_spill_count: 0
    .symbol:         _Z5k_gcnILi1EEvPKvPK15HIP_vector_typeIiLj2EEPfPKiS8_PKfPKDF16_SA_SA_SA_SA_S6_PDF16_S6_SD_SC_SA_.kd
    .uniform_work_group_size: 1
    .uses_dynamic_stack: false
    .vgpr_count:     58
    .vgpr_spill_count: 0
    .wavefront_size: 64
  - .agpr_count:     0
    .args:
      - .actual_access:  read_only
        .address_space:  global
        .offset:         0
        .size:           8
        .value_kind:     global_buffer
      - .actual_access:  read_only
        .address_space:  global
        .offset:         8
        .size:           8
        .value_kind:     global_buffer
      - .actual_access:  read_only
        .address_space:  global
        .offset:         16
        .size:           8
        .value_kind:     global_buffer
      - .actual_access:  read_only
        .address_space:  global
        .offset:         24
        .size:           8
        .value_kind:     global_buffer
      - .actual_access:  read_only
        .address_space:  global
        .offset:         32
        .size:           8
        .value_kind:     global_buffer
      - .actual_access:  read_only
        .address_space:  global
        .offset:         40
        .size:           8
        .value_kind:     global_buffer
      - .actual_access:  read_only
        .address_space:  global
        .offset:         48
        .size:           8
        .value_kind:     global_buffer
      - .actual_access:  read_only
        .address_space:  global
        .offset:         56
        .size:           8
        .value_kind:     global_buffer
      - .actual_access:  read_only
        .address_space:  global
        .offset:         64
        .size:           8
        .value_kind:     global_buffer
      - .actual_access:  read_only
        .address_space:  global
        .offset:         72
        .size:           8
        .value_kind:     global_buffer
      - .actual_access:  read_only
        .address_space:  global
        .offset:         80
        .size:           8
        .value_kind:     global_buffer
      - .actual_access:  read_only
        .address_space:  global
        .offset:         88
        .size:           8
        .value_kind:     global_buffer
      - .actual_access:  write_only
        .address_space:  global
        .offset:         96
        .size:           8
        .value_kind:     global_buffer
      - .address_space:  global
        .offset:         104
        .size:           8
        .value_kind:     global_buffer
      - .actual_access:  read_only
        .address_space:  global
        .offset:         112
        .size:           8
        .value_kind:     global_buffer
      - .actual_access:  read_only
        .address_space:  global
        .offset:         120
        .size:           8
        .value_kind:     global_buffer
      - .actual_access:  read_only
        .address_space:  global
        .offset:         128
        .size:           8
        .value_kind:     global_buffer
      - .offset:         136
        .size:           4
        .value_kind:     hidden_block_count_x
      - .offset:         140
        .size:           4
        .value_kind:     hidden_block_count_y
      - .offset:         144
        .size:           4
        .value_kind:     hidden_block_count_z
      - .offset:         148
        .size:           2
        .value_kind:     hidden_group_size_x
      - .offset:         150
        .size:           2
        .value_kind:     hidden_group_size_y
      - .offset:         152
        .size:           2
        .value_kind:     hidden_group_size_z
      - .offset:         154
        .size:           2
        .value_kind:     hidden_remainder_x
      - .offset:         156
        .size:           2
        .value_kind:     hidden_remainder_y
      - .offset:         158
        .size:           2
        .value_kind:     hidden_remainder_z
      - .offset:         176
        .size:           8
        .value_kind:     hidden_global_offset_x
      - .offset:         184
        .size:           8
        .value_kind:     hidden_global_offset_y
      - .offset:         192
        .size:           8
        .value_kind:     hidden_global_offset_z
      - .offset:         200
        .size:           2
        .value_kind:     hidden_grid_dims
    .group_segment_fixed_size: 23808
    .kernarg_segment_align: 8
    .kernarg_segment_size: 392
    .language:       OpenCL C
    .language_version:
      - 2
      - 0
    .max_flat_workgroup_size: 256
    .name:           _Z5k_gcnILi2EEvPKvPK15HIP_vector_typeIiLj2EEPfPKiS8_PKfPKDF16_SA_SA_SA_SA_S6_PDF16_S6_SD_SC_SA_
    .private_segment_fixed_size: 0
    .sgpr_count:     36
    .sgpr_spill_count: 0
    .symbol:         _Z5k_gcnILi2EEvPKvPK15HIP_vector_typeIiLj2EEPfPKiS8_PKfPKDF16_SA_SA_SA_SA_S6_PDF16_S6_SD_SC_SA_.kd
    .uniform_work_group_size: 1
    .uses_dynamic_stack: false
    .vgpr_count:     128
    .vgpr_spill_count: 0
    .wavefront_size: 64
  - .agpr_count:     0
    .args:
      - .actual_access:  read_only
        .address_space:  global
        .offset:         0
        .size:           8
        .value_kind:     global_buffer
      - .actual_access:  read_only
        .address_space:  global
        .offset:         8
        .size:           8
        .value_kind:     global_buffer
      - .actual_access:  read_only
        .address_space:  global
        .offset:         16
        .size:           8
        .value_kind:     global_buffer
      - .actual_access:  read_only
        .address_space:  global
        .offset:         24
        .size:           8
        .value_kind:     global_buffer
      - .actual_access:  write_only
        .address_space:  global
        .offset:         32
        .size:           8
        .value_kind:     global_buffer
      - .actual_access:  read_only
        .address_space:  global
        .offset:         40
        .size:           8
        .value_kind:     global_buffer
      - .actual_access:  read_only
        .address_space:  global
        .offset:         48
        .size:           8
        .value_kind:     global_buffer
      - .actual_access:  read_only
        .address_space:  global
        .offset:         56
        .size:           8
        .value_kind:     global_buffer
      - .actual_access:  read_only
        .address_space:  global
        .offset:         64
        .size:           8
        .value_kind:     global_buffer
      - .actual_access:  read_only
        .address_space:  global
        .offset:         72
        .size:           8
        .value_kind:     global_buffer
      - .actual_access:  read_only
        .address_space:  global
        .offset:         80
        .size:           8
        .value_kind:     global_buffer
      - .actual_access:  read_only
        .address_space:  global
        .offset:         88
        .size:           8
        .value_kind:     global_buffer
      - .actual_access:  write_only
        .address_space:  global
        .offset:         96
        .size:           8
        .value_kind:     global_buffer
    .group_segment_fixed_size: 9216
    .kernarg_segment_align: 8
    .kernarg_segment_size: 104
    .language:       OpenCL C
    .language_version:
      - 2
      - 0
    .max_flat_workgroup_size: 512
    .name:           _Z6k_lstmILi256ELi10ELb1ELb0EEvPKDF16_S1_S1_PKfPDF16_S1_S1_S1_S3_S3_S3_PfS5_
    .private_segment_fixed_size: 0
    .sgpr_count:     37
    .sgpr_spill_count: 0
    .symbol:         _Z6k_lstmILi256ELi10ELb1ELb0EEvPKDF16_S1_S1_PKfPDF16_S1_S1_S1_S3_S3_S3_PfS5_.kd
    .uniform_work_group_size: 1
    .uses_dynamic_stack: false
    .vgpr_count:     256
    .vgpr_spill_count: 0
    .wavefront_size: 64
  - .agpr_count:     0
    .args:
      - .actual_access:  read_only
        .address_space:  global
        .offset:         0
        .size:           8
        .value_kind:     global_buffer
      - .actual_access:  read_only
        .address_space:  global
        .offset:         8
        .size:           8
        .value_kind:     global_buffer
      - .actual_access:  read_only
        .address_space:  global
        .offset:         16
        .size:           8
        .value_kind:     global_buffer
      - .actual_access:  read_only
        .address_space:  global
        .offset:         24
        .size:           8
        .value_kind:     global_buffer
      - .actual_access:  read_only
        .address_space:  global
        .offset:         32
        .size:           8
        .value_kind:     global_buffer
      - .actual_access:  read_only
        .address_space:  global
        .offset:         40
        .size:           8
        .value_kind:     global_buffer
      - .actual_access:  read_only
        .address_space:  global
        .offset:         48
        .size:           8
        .value_kind:     global_buffer
      - .actual_access:  read_only
        .address_space:  global
        .offset:         56
        .size:           8
        .value_kind:     global_buffer
      - .actual_access:  read_only
        .address_space:  global
        .offset:         64
        .size:           8
        .value_kind:     global_buffer
      - .actual_access:  read_only
        .address_space:  global
        .offset:         72
        .size:           8
        .value_kind:     global_buffer
      - .actual_access:  read_only
        .address_space:  global
        .offset:         80
        .size:           8
        .value_kind:     global_buffer
      - .actual_access:  write_only
        .address_space:  global
        .offset:         88
        .size:           8
        .value_kind:     global_buffer
      - .actual_access:  read_only
        .address_space:  global
        .offset:         96
        .size:           8
        .value_kind:     global_buffer
    .group_segment_fixed_size: 0
    .kernarg_segment_align: 8
    .kernarg_segment_size: 104
    .language:       OpenCL C
    .language_version:
      - 2
      - 0
    .max_flat_workgroup_size: 512
    .name:           _Z6k_lstmILi128ELi8ELb0ELb1EEvPKDF16_S1_S1_PKfPDF16_S1_S1_S1_S3_S3_S3_PfS5_
    .private_segment_fixed_size: 0
    .sgpr_count:     46
    .sgpr_spill_count: 0
    .symbol:         _Z6k_lstmILi128ELi8ELb0ELb1EEvPKDF16_S1_S1_PKfPDF16_S1_S1_S1_S3_S3_S3_PfS5_.kd
    .uniform_work_group_size: 1
    .uses_dynamic_stack: false
    .vgpr_count:     256
    .vgpr_spill_count: 0
    .wavefront_size: 64
